# v73 with the whole instruction stream shifted by +4 bytes (one s_nop at entry): code-placement phase check
# speedup vs baseline: 1.0035x; 1.0035x over previous
; #define LAS __attribute__((address_space(3)))
; DI KParamsPtr kparams() { KParamsPtr p = (KParamsPtr)__builtin_amdgcn_kernarg_segment_ptr(); asm volatile("" : "+s"(p)); return p; }
; DI unsigned xb_add(unsigned* p, unsigned v) { return __hip_atomic_fetch_add(p, v, __ATOMIC_RELAXED, __HIP_MEMORY_SCOPE_AGENT); }
; DI unsigned xb_xcc_id() { return (unsigned)__builtin_amdgcn_s_getreg((3 << 11) | 20) & 0xFu; }
; DI XcdBarrier xcd_barrier_post(unsigned* bar, volatile LAS unsigned* st) {
;     XcdBarrier b; b.bar = bar; b.x = xb_xcc_id(); b.st = st;
;     if (threadIdx.x == 0) (void)xb_add(&bar[XB_XCNT(b.x)], 1u);
;     return b;
; __global__ void __launch_bounds__(512, 2) mega(Params Pdummy) {
;     ...
;     if (threadIdx.x < 4) ((LAS unsigned*)(ldsL + LDS_BARW))[threadIdx.x] = 0u;
;     __syncthreads();
;     { KParamsPtr kp = kparams(); (void)xcd_barrier_post((unsigned*)(kp->ws + WS_BAR), (volatile LAS unsigned*)(ldsL + LDS_BARW)); }
_Z4mega6Params:
	s_nop 0
	v_cmp_gt_u32_e32 vcc, 4, v0
	s_and_saveexec_b64 s[4:5], vcc
	v_lshl_add_u32 v1, v0, 2, 0
	v_add_u32_e32 v1, 0x21000, v1
	v_mov_b32_e32 v2, 0
	ds_write_b32 v1, v2
	s_or_b64 exec, exec, s[4:5]
	s_mov_b64 s[6:7], s[0:1]
	s_waitcnt lgkmcnt(0)
	s_barrier
	s_getreg_b32 s3, hwreg(HW_REG_XCC_ID, 0, 4)
	v_cmp_eq_u32_e64 s[90:91], 0, v0
	s_and_saveexec_b64 s[4:5], s[90:91]
	s_cbranch_execz .LBB0_5
	s_mov_b64 s[8:9], exec
	v_mbcnt_lo_u32_b32 v1, s8, 0
	v_mbcnt_hi_u32_b32 v1, s9, v1
	v_cmp_eq_u32_e32 vcc, 0, v1
	s_and_b64 s[10:11], exec, vcc
	s_mov_b64 exec, s[10:11]
	s_cbranch_execz .LBB0_5
	s_load_dwordx2 s[6:7], s[6:7], 0xd8
	s_lshl_b32 s3, s3, 8
	s_and_b32 s3, s3, 0xf00
	s_bcnt1_i32_b64 s8, s[8:9]
	v_mov_b32_e32 v1, s3
	v_mov_b32_e32 v2, s8
	s_waitcnt lgkmcnt(0)
	global_atomic_add v1, v2, s[6:7] offset:1024
